# XATT K/V staging by direct HBM->LDS loads (per-lane chunk addresses reproduce the swizzled K and v_st V layouts; 16 loads in flight, no VGPR staging or ds_write)
# baseline (speedup 1.0000x reference)
; __device__ __forceinline__ int v_st(int k, int c) { const int kk = (k & ~0xC) | ((k & 4) << 1) | ((k & 8) >> 1); return ((kk >> 3) * 4 + (c >> 5)) * 512 + ((kk & 7) * 32 + (c & 31)) * 2; }
; __device__ __forceinline__ int v_rd_base(int lane) { return ((lane & 3) << 3) | (((lane >> 2) & 3) << 6) | (((lane >> 4) & 1) << 5) | (((lane >> 5) & 1) << 8); }
; #define ATT_LOAD(X, t) do { const int _j = 64 * (t) + sr; ks##X##0 = *(const bf16x8*)(c.k_ptr(_j) + sc); vs##X##0 = *(const bf16x8*)(c.v_ptr(_j) + sc); \
;         if (D128) { ks##X##1 = *(const bf16x8*)(c.k_ptr(_j + 32) + sc); vs##X##1 = *(const bf16x8*)(c.v_ptr(_j + 32) + sc); } } while (0)
; #define ATT_WRITE(X, b) do { *(LAS bf16x8*)(V_lds + (b) * SHM_T + vst0) = vs##X##0; *(LAS bf16x8*)(K_lds + (b) * SHM_T + kst0) = ks##X##0; \
;         if (D128) { *(LAS bf16x8*)(V_lds + (b) * SHM_T + vst1) = vs##X##1; *(LAS bf16x8*)(K_lds + (b) * SHM_T + kst1) = ks##X##1; } } while (0)
; #define ATT_LOAD(t) do { _Pragma("unroll") for (int p_ = 0; p_ < 4; ++p_) { const int _j = 64 * (t) + sr + 16 * p_; ks[p_] = *(const bf16x8*)(c.k_ptr(_j) + sc); vs[p_] = *(const bf16x8*)(c.v_ptr(_j) + sc); } } while (0)
; #define ATT_WRITE(b) do { _Pragma("unroll") for (int p_ = 0; p_ < 4; ++p_) { *(LAS bf16x8*)(V_lds + (b) * SHM_T + v_st(sr + 16 * p_, sc)) = vs[p_]; *(LAS bf16x8*)(K_lds + (b) * SHM_T + ATT_KSWZ(sr + 16 * p_, sc * 2)) = ks[p_]; } } while (0)
; template <int DK16, int DV32, bool MASK, int HALFWIN, bool RES, bool WT, class P>
; __device__ __forceinline__ void attn_unit(LAS unsigned char* lds, const P& c, const int ntiles, const float C, const int wv) {
;     ...
;     const int sr = D128 ? (tid >> 4) : (tid >> 3), sc = D128 ? (tid & 15) * 8 : (tid & 7) * 8;
;     const int vst0 = v_st(sr, sc), vst1 = v_st(32 + sr, sc), kst0 = ATT_KSWZ(sr, sc * 2), kst1 = ATT_KSWZ(32 + sr, sc * 2);
;     const int vb0 = (int)(unsigned)(uintptr_t)V_lds + v_rd_base(lane);
;     bf16x8 ksA0, ksA1, vsA0, vsA1, ksB0, ksB1, vsB0, vsB1;
;     ...
;     if constexpr (RES) {
;         ATT_LOAD(A, 0); ATT_LOAD(B, 1); ATT_WRITE(A, 0); ATT_LOAD(A, 2); ATT_WRITE(B, 1); ATT_LOAD(B, 3); ATT_WRITE(A, 2); ATT_WRITE(B, 3);
;         __syncthreads();
;         compute(0, 0); compute(1, 1); compute(2, 2); compute(3, 3);
;         __syncthreads();
.LBB0_1197:
	s_ashr_i32 s1, s0, 31
	s_lshl_b64 s[0:1], s[0:1], 19
	s_add_u32 s0, s6, s0
	s_addc_u32 s1, s7, s1
	s_barrier
	v_mbcnt_lo_u32_b32 v0, -1, 0
	v_mbcnt_hi_u32_b32 v0, -1, v0
	s_add_u32 s0, s0, 0x21700000
	v_add_u32_e32 v154, s93, v0
	s_addc_u32 s1, s1, 0
	s_waitcnt lgkmcnt(0)
	v_readfirstlane_b32 s3, v154
	s_lshl_b32 s8, s17, 8
	s_ashr_i32 s11, s3, 6
	v_and_b32_e32 v156, 31, v154
	s_lshl_b32 s3, s11, 8
	s_lshl_b32 s9, s11, 5
	v_or_b32_e32 v0, s8, v156
	s_and_b32 s2, s16, 0xffffff80
	s_add_i32 s10, s3, 0x100
	v_add_u32_e32 v0, s9, v0
	s_lshl_b32 s3, s15, 8
	v_ashrrev_i32_e32 v1, 31, v0
	s_add_i32 s2, s3, s2
	v_lshlrev_b64 v[0:1], 10, v[0:1]
	s_ashr_i32 s3, s2, 31
	v_lshl_add_u64 v[0:1], s[6:7], 0, v[0:1]
	s_lshl_b64 s[4:5], s[2:3], 1
	v_lshrrev_b32_e32 v32, 1, v154
	v_lshl_add_u64 v[0:1], v[0:1], 0, s[4:5]
	v_and_b32_e32 v64, 16, v32
	v_lshl_add_u64 v[0:1], v[0:1], 0, v[64:65]
	s_mov_b64 s[16:17], 0x8100000
	s_mov_b32 s15, 0x8100000
	v_lshl_add_u64 v[2:3], v[0:1], 0, s[16:17]
	v_add_co_u32_e32 v0, vcc, s15, v0
	v_mov_b32_e32 v9, v65
	s_nop 0
	v_addc_co_u32_e32 v1, vcc, 0, v1, vcc
	global_load_dwordx4 v[126:129], v[0:1], off
	global_load_dwordx4 v[122:125], v[2:3], off offset:32
	global_load_dwordx4 v[118:121], v[2:3], off offset:64
	global_load_dwordx4 v[114:117], v[2:3], off offset:96
	global_load_dwordx4 v[110:113], v[2:3], off offset:128
	global_load_dwordx4 v[106:109], v[2:3], off offset:160
	global_load_dwordx4 v[102:105], v[2:3], off offset:192
	global_load_dwordx4 v[98:101], v[2:3], off offset:224
	v_lshrrev_b32_e32 v0, 4, v154
	v_and_b32_e32 v2, 15, v154
	v_and_b32_e32 v1, 7, v0
	v_xor_b32_e32 v1, v1, v2
	v_lshlrev_b32_e32 v1, 4, v1
	v_lshl_add_u32 v0, v0, 11, v1
	v_bfe_u32 v2, v154, 2, 3
	v_lshrrev_b32_e32 v3, 6, v154
	v_lshl_or_b32 v2, v3, 3, v2
	v_and_b32_e32 v3, 4, v2
	v_and_b32_e32 v4, 8, v2
	v_lshlrev_b32_e32 v3, 1, v3
	v_lshrrev_b32_e32 v4, 1, v4
	v_and_b32_e32 v2, 0x33, v2
	v_or3_b32 v2, v2, v3, v4
	v_bfe_u32 v3, v154, 5, 1
	v_and_b32_e32 v4, 3, v154
	v_lshlrev_b32_e32 v3, 6, v3
	v_lshl_or_b32 v3, v4, 4, v3
	v_lshl_add_u32 v1, v2, 11, v3
	v_add_u32_e32 v2, 0x80, v1
	s_add_u32 s0, s0, s4
	s_addc_u32 s1, s1, s5
	v_readfirstlane_b32 s58, v154
	s_lshr_b32 s58, s58, 6
	s_lshl_b32 s60, s58, 11
	s_lshl_b32 s58, s58, 10
	s_add_i32 s46, s91, 0x100
	s_add_i32 s47, s92, 0x100
	s_add_i32 s52, s65, 0x100
	s_add_i32 s53, s71, 0x100
	s_add_i32 s64, s46, s58
	s_add_u32 s48, s0, 0x10000
	s_mov_b32 m0, s64
	s_addc_u32 s49, s1, 0
	global_load_lds_dwordx4 v0, s[0:1]
	s_addk_i32 s64, 0x2000
	s_mov_b32 m0, s64
	s_nop 0
	global_load_lds_dwordx4 v0, s[48:49]
	s_add_i32 s64, s60, 0x100
	s_add_u32 s48, s0, 0x400
	s_mov_b32 m0, s64
	s_addc_u32 s49, s1, 0
	global_load_lds_dwordx4 v1, s[48:49]
	s_addk_i32 s64, 0x400
	s_mov_b32 m0, s64
	s_nop 0
	global_load_lds_dwordx4 v2, s[48:49]
	s_add_u32 s0, s0, 0x20000
	s_addc_u32 s1, s1, 0
	s_add_i32 s64, s47, s58
	s_add_u32 s48, s0, 0x10000
	s_mov_b32 m0, s64
	s_addc_u32 s49, s1, 0
	global_load_lds_dwordx4 v0, s[0:1]
	s_addk_i32 s64, 0x2000
	s_mov_b32 m0, s64
	s_nop 0
	global_load_lds_dwordx4 v0, s[48:49]
	s_add_i32 s64, s60, 0x4100
	s_add_u32 s48, s0, 0x400
	s_mov_b32 m0, s64
	s_addc_u32 s49, s1, 0
	global_load_lds_dwordx4 v1, s[48:49]
	s_addk_i32 s64, 0x400
	s_mov_b32 m0, s64
	s_nop 0
	global_load_lds_dwordx4 v2, s[48:49]
	s_add_u32 s0, s0, 0x20000
	s_addc_u32 s1, s1, 0
	s_add_i32 s64, s52, s58
	s_add_u32 s48, s0, 0x10000
	s_mov_b32 m0, s64
	s_addc_u32 s49, s1, 0
	global_load_lds_dwordx4 v0, s[0:1]
	s_addk_i32 s64, 0x2000
	s_mov_b32 m0, s64
	s_nop 0
	global_load_lds_dwordx4 v0, s[48:49]
	s_add_i32 s64, s60, 0x8100
	s_add_u32 s48, s0, 0x400
	s_mov_b32 m0, s64
	s_addc_u32 s49, s1, 0
	global_load_lds_dwordx4 v1, s[48:49]
	s_addk_i32 s64, 0x400
	s_mov_b32 m0, s64
	s_nop 0
	global_load_lds_dwordx4 v2, s[48:49]
	s_add_u32 s0, s0, 0x20000
	s_addc_u32 s1, s1, 0
	s_add_i32 s64, s53, s58
	s_add_u32 s48, s0, 0x10000
	s_mov_b32 m0, s64
	s_addc_u32 s49, s1, 0
	global_load_lds_dwordx4 v0, s[0:1]
	s_addk_i32 s64, 0x2000
	s_mov_b32 m0, s64
	s_nop 0
	global_load_lds_dwordx4 v0, s[48:49]
	s_add_i32 s64, s60, 0xc100
	s_add_u32 s48, s0, 0x400
	s_mov_b32 m0, s64
	s_addc_u32 s49, s1, 0
	global_load_lds_dwordx4 v1, s[48:49]
	s_addk_i32 s64, 0x400
	s_mov_b32 m0, s64
	s_nop 0
	global_load_lds_dwordx4 v2, s[48:49]
	v_lshlrev_b32_e32 v168, 8, v156
	v_and_b32_e32 v155, 63, v154
	s_add_i32 s10, s10, 0x20400
	v_cmp_gt_u32_e64 s[4:5], 32, v155
	s_movk_i32 s0, 0x60
	v_lshlrev_b32_e32 v0, 4, v154
	v_and_b32_e32 v0, 0x70, v0
	v_bitop3_b32 v164, v64, v0, s0 bitop3:0x36
	s_movk_i32 s0, 0x80
	v_bitop3_b32 v165, v64, v0, s0 bitop3:0x36
	s_movk_i32 s0, 0xa0
	v_bitop3_b32 v166, v64, v0, s0 bitop3:0x36
	s_movk_i32 s0, 0xc0
	v_bitop3_b32 v167, v64, v0, s0 bitop3:0x36
	s_movk_i32 s0, 0xe0
	v_add_u32_e32 v1, s46, v168
	v_bitop3_b32 v169, v32, v0, 16 bitop3:0x6c
	v_bitop3_b32 v162, v64, v0, 32 bitop3:0x36
	v_bitop3_b32 v163, v64, v0, 64 bitop3:0x36
	v_bitop3_b32 v161, v64, v0, s0 bitop3:0x36
	v_add_u32_e32 v2, v1, v169
	v_add_u32_e32 v20, v1, v162
	v_add_u32_e32 v24, v1, v163
	v_add_u32_e32 v25, v1, v164
	v_add_u32_e32 v26, v1, v165
	v_add_u32_e32 v27, v1, v166
	v_add_u32_e32 v28, v1, v167
	v_add_u32_e32 v29, v1, v161
	s_waitcnt vmcnt(0)
	s_waitcnt lgkmcnt(0)
	s_barrier
; template <int DK16, int DV32, bool MASK, int HALFWIN, bool RES, bool WT, class P>
; __device__ __forceinline__ void attn_unit(LAS unsigned char* lds, const P& c, const int ntiles, const float C, const int wv) {
;     ...
;             if (do0) {
; #pragma unroll
;                 for (int d0 = 0; d0 < DK16; ++d0) { const bf16x8 b0 = *(const LAS bf16x8*)(Ks + ATT_KSWZ(r32, (d0 * 16 + hi * 8) * 2)); p0 = __builtin_amdgcn_mfma_f32_32x32x16_bf16(b0, qr[d0], p0, 0, 0, 0); } }
;             if (do1) {
; #pragma unroll
;                 for (int d0 = 0; d0 < DK16; ++d0) { const bf16x8 b1 = *(const LAS bf16x8*)(Ks + ATT_KSWZ(32 + r32, (d0 * 16 + hi * 8) * 2)); p1 = __builtin_amdgcn_mfma_f32_32x32x16_bf16(b1, qr[d0], p1, 0, 0, 0); } }
;             if constexpr (MASK) {
;                 const int db = c.dbase(wid, r32, t) + 4 * hi, qi = c.qidx(wid, r32); const unsigned L = (unsigned)c.seqlen(); const bool edge = c.edge();
;                 const LAS float* tb = c.tab(wid) + (db + 2 * HALFWIN);
;     ...
;                 if (do0) ATT_XFORM(p0, 0);
;                 if (do1) ATT_XFORM(p1, 32);
;     ...
;             } else {
; #pragma unroll
;                 for (int r = 0; r < 16; ++r) { p0[r] *= C; p1[r] *= C; }
;             }
;             float pmax = -__builtin_inff();
;             if (do0) {
; #pragma unroll
;                 for (int r = 0; r < 16; ++r) pmax = fmaxf(pmax, p0[r]); }
;             if (do1) {
; #pragma unroll
;                 for (int r = 0; r < 16; ++r) pmax = fmaxf(pmax, p1[r]); }
;             { auto rr = __builtin_amdgcn_permlane32_swap(__float_as_uint(pmax), __float_as_uint(pmax), false, false);
;               pmax = fmaxf(__uint_as_float(rr[0]), __uint_as_float(rr[1])); }
;             const float mn = fmaxf(m_reg, pmax), alpha = __builtin_amdgcn_exp2f(m_reg - mn); m_reg = mn;
;             float ps = 0.f;
;             if (do0) {
; #pragma unroll
;                 for (int r = 0; r < 16; ++r) { p0[r] = __builtin_amdgcn_exp2f(p0[r] - mn); ps += p0[r]; } }
;             if (do1) {
; #pragma unroll
;                 for (int r = 0; r < 16; ++r) { p1[r] = __builtin_amdgcn_exp2f(p1[r] - mn); ps += p1[r]; } }
;             { auto rr = __builtin_amdgcn_permlane32_swap(__float_as_uint(ps), __float_as_uint(ps), false, false);
;               ps = __uint_as_float(rr[0]) + __uint_as_float(rr[1]); }
;             l_reg = l_reg * alpha + ps;
	ds_read_b128 v[16:19], v2
	ds_read_b128 v[32:35], v20
	ds_read_b128 v[36:39], v24
	ds_read_b128 v[40:43], v25
	ds_read_b128 v[44:47], v26
	ds_read_b128 v[48:51], v27
	ds_read_b128 v[52:55], v28
	ds_read_b128 v[56:59], v29
	ds_read_b128 v[0:3], v2 offset:8192
	ds_read_b128 v[20:23], v20 offset:8192
	s_waitcnt lgkmcnt(1)
	v_mfma_f32_32x32x16_bf16 v[0:15], v[0:3], v[126:129], 0
	s_mov_b32 s0, 0xf149f2ca
	s_waitcnt lgkmcnt(0)
	v_mfma_f32_32x32x16_bf16 v[0:15], v[20:23], v[122:125], v[0:15]
	ds_read_b128 v[20:23], v24 offset:8192
	s_waitcnt lgkmcnt(0)
	v_mfma_f32_32x32x16_bf16 v[0:15], v[20:23], v[118:121], v[0:15]
	ds_read_b128 v[20:23], v25 offset:8192
	s_waitcnt lgkmcnt(0)
	v_mfma_f32_32x32x16_bf16 v[0:15], v[20:23], v[114:117], v[0:15]
	ds_read_b128 v[20:23], v26 offset:8192
	s_waitcnt lgkmcnt(0)
	v_mfma_f32_32x32x16_bf16 v[0:15], v[20:23], v[110:113], v[0:15]
	ds_read_b128 v[20:23], v27 offset:8192
	s_waitcnt lgkmcnt(0)
	v_mfma_f32_32x32x16_bf16 v[0:15], v[20:23], v[106:109], v[0:15]
	ds_read_b128 v[20:23], v28 offset:8192
	s_waitcnt lgkmcnt(0)
	v_mfma_f32_32x32x16_bf16 v[0:15], v[20:23], v[102:105], v[0:15]
	ds_read_b128 v[20:23], v29 offset:8192
	s_waitcnt lgkmcnt(0)
	v_mfma_f32_32x32x16_bf16 v[0:15], v[20:23], v[98:101], v[0:15]
	v_mfma_f32_32x32x16_bf16 v[16:31], v[16:19], v[126:129], 0
	s_nop 10
	v_mul_f32_e32 v61, 0x3e0293ee, v14
	v_mul_f32_e32 v63, 0x3e0293ee, v15
	v_mfma_f32_32x32x16_bf16 v[16:31], v[32:35], v[122:125], v[16:31]
	v_mul_f32_e32 v33, 0x3e0293ee, v0
	v_mul_f32_e32 v35, 0x3e0293ee, v1
	v_mfma_f32_32x32x16_bf16 v[16:31], v[36:39], v[118:121], v[16:31]
	v_mul_f32_e32 v37, 0x3e0293ee, v2
	v_mul_f32_e32 v39, 0x3e0293ee, v3
	v_mfma_f32_32x32x16_bf16 v[16:31], v[40:43], v[114:117], v[16:31]
	v_mul_f32_e32 v41, 0x3e0293ee, v4
	v_mul_f32_e32 v43, 0x3e0293ee, v5
	v_mfma_f32_32x32x16_bf16 v[16:31], v[44:47], v[110:113], v[16:31]
	v_mul_f32_e32 v45, 0x3e0293ee, v6
	v_mul_f32_e32 v47, 0x3e0293ee, v7
	v_mfma_f32_32x32x16_bf16 v[16:31], v[48:51], v[106:109], v[16:31]
	v_mul_f32_e32 v49, 0x3e0293ee, v8
	v_mul_f32_e32 v51, 0x3e0293ee, v9
	v_mfma_f32_32x32x16_bf16 v[16:31], v[52:55], v[102:105], v[16:31]
	v_mul_f32_e32 v53, 0x3e0293ee, v10
	v_mul_f32_e32 v55, 0x3e0293ee, v11
	v_mfma_f32_32x32x16_bf16 v[16:31], v[56:59], v[98:101], v[16:31]
	v_mul_f32_e32 v57, 0x3e0293ee, v12
	v_mul_f32_e32 v59, 0x3e0293ee, v13
	s_nop 9
	v_mul_f32_e32 v32, 0x3e0293ee, v16
	v_mul_f32_e32 v34, 0x3e0293ee, v17
	v_mul_f32_e32 v36, 0x3e0293ee, v18
	v_mul_f32_e32 v38, 0x3e0293ee, v19
	v_max3_f32 v32, v32, s38, v34
	v_mul_f32_e32 v40, 0x3e0293ee, v20
	v_mul_f32_e32 v42, 0x3e0293ee, v21
	v_max3_f32 v32, v32, v36, v38
	v_mul_f32_e32 v44, 0x3e0293ee, v22
	v_mul_f32_e32 v46, 0x3e0293ee, v23
	v_max3_f32 v32, v32, v40, v42
	v_mul_f32_e32 v48, 0x3e0293ee, v24
	v_mul_f32_e32 v50, 0x3e0293ee, v25
	v_max3_f32 v32, v32, v44, v46
	v_mul_f32_e32 v52, 0x3e0293ee, v26
	v_mul_f32_e32 v54, 0x3e0293ee, v27
	v_max3_f32 v32, v32, v48, v50
	v_mul_f32_e32 v56, 0x3e0293ee, v28
	v_mul_f32_e32 v58, 0x3e0293ee, v29
	v_max3_f32 v32, v32, v52, v54
	v_mul_f32_e32 v60, 0x3e0293ee, v30
	v_mul_f32_e32 v62, 0x3e0293ee, v31
	v_max3_f32 v32, v32, v56, v58
	v_max3_f32 v32, v32, v60, v62
	v_max3_f32 v32, v32, v33, v35
	v_max3_f32 v32, v32, v37, v39
	v_max3_f32 v32, v32, v41, v43
	v_max3_f32 v32, v32, v45, v47
	v_max3_f32 v32, v32, v49, v51
	v_max3_f32 v32, v32, v53, v55
	v_max3_f32 v32, v32, v57, v59
	v_max3_f32 v32, v32, v61, v63
	v_mov_b32_e32 v33, v32
	s_nop 1
	v_permlane32_swap_b32_e32 v32, v33
	v_max3_f32 v171, v32, v33, s0
	v_fma_f32 v16, v16, s94, -v171
	v_exp_f32_e32 v16, v16
	v_fma_f32 v17, v17, s94, -v171
	v_exp_f32_e32 v17, v17
	v_fma_f32 v18, v18, s94, -v171
	v_exp_f32_e32 v18, v18
	v_fma_f32 v19, v19, s94, -v171
	v_exp_f32_e32 v19, v19
	v_fma_f32 v20, v20, s94, -v171
	v_add_f32_e32 v33, 0, v16
	v_exp_f32_e32 v20, v20
	v_fma_f32 v21, v21, s94, -v171
	v_add_f32_e32 v33, v17, v33
	v_exp_f32_e32 v21, v21
	v_fma_f32 v22, v22, s94, -v171
	v_add_f32_e32 v33, v18, v33
	v_exp_f32_e32 v22, v22
	v_fma_f32 v23, v23, s94, -v171
	v_add_f32_e32 v33, v19, v33
	v_exp_f32_e32 v23, v23
	v_fma_f32 v24, v24, s94, -v171
	v_add_f32_e32 v33, v20, v33
	v_exp_f32_e32 v24, v24
	v_fma_f32 v25, v25, s94, -v171
	v_add_f32_e32 v33, v21, v33
	v_exp_f32_e32 v25, v25
	v_fma_f32 v26, v26, s94, -v171
	v_add_f32_e32 v33, v22, v33
	v_exp_f32_e32 v26, v26
	v_fma_f32 v27, v27, s94, -v171
	v_add_f32_e32 v33, v23, v33
	v_exp_f32_e32 v27, v27
	v_fma_f32 v28, v28, s94, -v171
	v_add_f32_e32 v33, v24, v33
	v_exp_f32_e32 v28, v28
	v_fma_f32 v29, v29, s94, -v171
	v_add_f32_e32 v33, v25, v33
	v_exp_f32_e32 v29, v29
	v_fma_f32 v30, v30, s94, -v171
	v_add_f32_e32 v33, v26, v33
	v_exp_f32_e32 v30, v30
	v_fma_f32 v31, v31, s94, -v171
	v_add_f32_e32 v33, v27, v33
	v_exp_f32_e32 v31, v31
	v_fma_f32 v0, v0, s94, -v171
	v_add_f32_e32 v33, v28, v33
	v_exp_f32_e32 v48, v0
	v_fma_f32 v1, v1, s94, -v171
	v_add_f32_e32 v33, v29, v33
	v_exp_f32_e32 v49, v1
	v_fma_f32 v1, v2, s94, -v171
	v_add_f32_e32 v33, v30, v33
	v_exp_f32_e32 v50, v1
	v_fma_f32 v1, v3, s94, -v171
	v_add_f32_e32 v33, v31, v33
	v_exp_f32_e32 v51, v1
	v_fma_f32 v1, v4, s94, -v171
	v_add_f32_e32 v0, v48, v33
	v_exp_f32_e32 v52, v1
	v_fma_f32 v1, v5, s94, -v171
	v_add_f32_e32 v0, v49, v0
	v_exp_f32_e32 v53, v1
	v_fma_f32 v1, v6, s94, -v171
	v_add_f32_e32 v0, v50, v0
	v_exp_f32_e32 v66, v1
	v_fma_f32 v1, v7, s94, -v171
	v_add_f32_e32 v0, v51, v0
	v_exp_f32_e32 v67, v1
	v_fma_f32 v1, v8, s94, -v171
	v_add_f32_e32 v0, v52, v0
	v_exp_f32_e32 v68, v1
	v_fma_f32 v1, v9, s94, -v171
	v_add_f32_e32 v0, v53, v0
	v_exp_f32_e32 v69, v1
	v_fma_f32 v1, v10, s94, -v171
	v_add_f32_e32 v0, v66, v0
	v_exp_f32_e32 v70, v1
	v_fma_f32 v1, v11, s94, -v171
	v_add_f32_e32 v0, v67, v0
	v_exp_f32_e32 v71, v1
	v_fma_f32 v1, v12, s94, -v171
	v_add_f32_e32 v0, v68, v0
	v_exp_f32_e32 v72, v1
	v_fma_f32 v1, v13, s94, -v171
	v_add_f32_e32 v0, v69, v0
	v_exp_f32_e32 v73, v1
	v_fma_f32 v1, v14, s94, -v171
	v_add_f32_e32 v0, v70, v0
	v_exp_f32_e32 v74, v1
	v_fma_f32 v1, v15, s94, -v171
	v_add_f32_e32 v0, v71, v0
	v_exp_f32_e32 v75, v1
	v_sub_f32_e32 v32, 0xf149f2ca, v171
	v_add_f32_e32 v0, v72, v0
	v_add_f32_e32 v0, v73, v0
	v_exp_f32_e32 v157, v32
	v_add_f32_e32 v0, v74, v0
	v_add_f32_e32 v158, v75, v0
	v_mov_b32_e32 v159, v158
	s_nop 1
	v_permlane32_swap_b32_e32 v158, v159
	v_cmp_gt_f32_e32 vcc, 1.0, v157
	s_cbranch_vccz .LBB0_1201
; __device__ __forceinline__ int crow(int r, int hi) { return (r & 3) + 8 * (r >> 2) + 4 * hi; }
; template <int DK16, int DV32, bool MASK, int HALFWIN, bool RES, bool WT, class P>
; __device__ __forceinline__ void attn_unit(LAS unsigned char* lds, const P& c, const int ntiles, const float C, const int wv) {
;     ...
;             if (__any(alpha < 1.f)) { if (hi == 0) al_l[r32] = alpha; asm volatile("s_waitcnt lgkmcnt(0)" ::: "memory");
; #pragma unroll
;                 for (int r = 0; r < 16; ++r) { const float a = al_l[crow(r, hi)];
; #pragma unroll
;                     for (int d = 0; d < DV32; ++d) o[d][r] *= a; } }
	s_and_saveexec_b64 s[0:1], s[4:5]
	v_lshl_add_u32 v0, v156, 2, s10
	ds_write_b32 v0, v157 offset:128
	s_or_b64 exec, exec, s[0:1]
	s_waitcnt lgkmcnt(0)
	v_add_u32_e32 v8, s10, v64
	ds_read_b128 v[0:3], v8 offset:224
	ds_read_b128 v[4:7], v8 offset:192
	ds_read_b128 v[32:35], v8 offset:160
	ds_read_b128 v[36:39], v8 offset:128
	s_waitcnt lgkmcnt(3)
	v_pk_mul_f32 v[14:15], v[2:3], 0 op_sel_hi:[1,0]
	s_waitcnt lgkmcnt(2)
	v_pk_mul_f32 v[10:11], v[6:7], 0 op_sel_hi:[1,0]
	s_waitcnt lgkmcnt(1)
	v_pk_mul_f32 v[6:7], v[34:35], 0 op_sel_hi:[1,0]
	s_waitcnt lgkmcnt(0)
	v_pk_mul_f32 v[2:3], v[38:39], 0 op_sel_hi:[1,0]
	v_pk_mul_f32 v[12:13], v[0:1], 0 op_sel_hi:[1,0]
	v_pk_mul_f32 v[8:9], v[4:5], 0 op_sel_hi:[1,0]
	v_pk_mul_f32 v[4:5], v[32:33], 0 op_sel_hi:[1,0]
	v_pk_mul_f32 v[0:1], v[36:37], 0 op_sel_hi:[1,0]
	s_branch .LBB0_1202
